# v82 + N2M wave-half reorder: waves 4-7 do slot-zero/token routing before the fp8 expert-weight conversion loop
# speedup vs baseline: 1.0151x; 1.0151x over previous
.LBB0_1374:
	v_readlane_b32 s34, v252, 1
	v_readlane_b32 s35, v252, 2
	v_mbcnt_lo_u32_b32 v144, -1, 0
	v_mbcnt_hi_u32_b32 v144, -1, v144
	v_readlane_b32 s6, v252, 6
	v_readlane_b32 s2, v252, 7
	s_add_i32 s7, s6, s2
	s_cmp_lt_u32 s6, 4
	s_cbranch_scc1 .Ln2m_normal
	v_readlane_b32 s98, v255, 62
	s_cmp_lg_u32 s98, 0
	s_cbranch_scc1 .Ln2m_normal
	s_mov_b32 s98, 1
	v_writelane_b32 v255, s98, 62
	v_lshlrev_b32_e32 v8, 2, v144
	s_branch .LBB0_1381
.Ln2m_normal:
	s_cmp_gt_i32 s7, 0xa7ff
	v_lshlrev_b32_e32 v8, 2, v144
	s_cbranch_scc1 .LBB0_1381
	s_add_u32 s10, s34, 0x6400000
	s_addc_u32 s11, s35, 0
	s_lshl_b32 s2, s6, 14
	v_lshlrev_b32_e32 v2, 3, v144
	s_add_i32 s2, s2, 0
	v_ashrrev_i32_e32 v1, 3, v144
	v_and_b32_e32 v0, 28, v8
	s_movk_i32 s3, 0x84
	v_and_b32_e32 v2, 56, v2
	v_lshl_add_u32 v4, v0, 2, s2
	v_mul_lo_u32 v5, v1, s3
	v_mul_u32_u24_e32 v6, 0x84, v2
	v_lshlrev_b32_e32 v7, 2, v1
	v_add_u32_e32 v9, 8, v1
	v_add_u32_e32 v20, 16, v1
	v_add_u32_e32 v21, 24, v1
	v_mov_b32_e32 v3, v161
	v_add3_u32 v22, s2, v6, v7
	s_lshl_b32 s31, s7, 5
	s_lshl_b32 s33, s7, 1
	v_add_u32_e32 v23, v4, v5
	s_mov_b32 s38, s7
	s_branch .LBB0_1377

.LBB0_1381:
	v_readlane_b32 s98, v255, 62
	s_cmp_eq_u32 s98, 2
	s_cbranch_scc0 .Ln2m_z
	s_mov_b32 s98, 0
	v_writelane_b32 v255, s98, 62
	v_cmp_eq_u32_e64 s[36:37], 0, v144
	s_branch .Ln2m_sync

.LBB0_1395:
	s_or_b64 exec, exec, s[18:19]
	v_readlane_b32 s98, v255, 62
	s_cmp_eq_u32 s98, 1
	s_cbranch_scc0 .Ln2m_sync
	s_mov_b32 s98, 2
	v_writelane_b32 v255, s98, 62
	s_branch .LBB0_1374
.Ln2m_sync:
	s_waitcnt lgkmcnt(0)
	s_cmp_eq_u32 s6, 0
	s_waitcnt lgkmcnt(0)
	s_barrier
	s_cbranch_scc0 .LBB0_1399
	v_lshl_add_u32 v0, v144, 2, 0
	v_add_u32_e32 v2, 0x20800, v0
	ds_read_b32 v3, v2
	v_lshlrev_b64 v[0:1], v144, -1
	v_not_b32_e32 v0, v0
	v_not_b32_e32 v1, v1
	v_cmp_gt_i32_e64 s[54:55], 8, v144
	s_waitcnt lgkmcnt(0)
	v_cmp_eq_u32_e32 vcc, 0, v3
	s_bcnt1_i32_b64 s2, vcc
	v_cmp_eq_u32_e64 s[38:39], 5, v3
	v_and_b32_e32 v5, vcc_lo, v0
	v_and_b32_e32 v4, vcc_hi, v1
	v_bcnt_u32_b32 v5, v5, 0
	v_bcnt_u32_b32 v4, v4, v5
	v_cndmask_b32_e32 v4, 0, v4, vcc
	v_cmp_eq_u32_e32 vcc, 1, v3
	s_bcnt1_i32_b64 s3, vcc
	v_cmp_eq_u32_e64 s[40:41], 6, v3
	v_and_b32_e32 v6, vcc_lo, v0
	v_and_b32_e32 v5, vcc_hi, v1
	v_bcnt_u32_b32 v6, v6, 0
	v_bcnt_u32_b32 v5, v5, v6
	v_cndmask_b32_e32 v4, v4, v5, vcc
	v_cmp_eq_u32_e32 vcc, 2, v3
	s_bcnt1_i32_b64 s6, vcc
	v_cmp_eq_u32_e64 s[42:43], 7, v3
	v_and_b32_e32 v6, vcc_lo, v0
	v_and_b32_e32 v5, vcc_hi, v1
	v_bcnt_u32_b32 v6, v6, 0
	v_bcnt_u32_b32 v5, v5, v6
	v_cndmask_b32_e32 v4, v4, v5, vcc
	v_cmp_eq_u32_e32 vcc, 3, v3
	s_bcnt1_i32_b64 s7, vcc
	s_bcnt1_i32_b64 s11, s[38:39]
	v_and_b32_e32 v6, vcc_lo, v0
	v_and_b32_e32 v5, vcc_hi, v1
	v_bcnt_u32_b32 v6, v6, 0
	v_bcnt_u32_b32 v5, v5, v6
	v_cndmask_b32_e32 v4, v4, v5, vcc
	v_cmp_eq_u32_e32 vcc, 4, v3
	v_and_b32_e32 v3, s43, v1
	s_bcnt1_i32_b64 s10, vcc
	v_and_b32_e32 v6, vcc_lo, v0
	v_and_b32_e32 v5, vcc_hi, v1
	v_bcnt_u32_b32 v6, v6, 0
	v_bcnt_u32_b32 v5, v5, v6
	v_and_b32_e32 v6, s38, v0
	v_cndmask_b32_e32 v4, v4, v5, vcc
	v_and_b32_e32 v5, s39, v1
	v_bcnt_u32_b32 v6, v6, 0
	v_bcnt_u32_b32 v5, v5, v6
	v_and_b32_e32 v6, s40, v0
	v_cndmask_b32_e64 v4, v4, v5, s[38:39]
	v_and_b32_e32 v5, s41, v1
	v_bcnt_u32_b32 v6, v6, 0
	v_bcnt_u32_b32 v5, v5, v6
	v_cndmask_b32_e64 v4, v4, v5, s[40:41]
	v_and_b32_e32 v5, s42, v0
	v_bcnt_u32_b32 v5, v5, 0
	v_bcnt_u32_b32 v3, v3, v5
	v_cndmask_b32_e64 v3, v4, v3, s[42:43]
	ds_write_b32 v2, v3 offset:1024
	ds_read_b32 v3, v2 offset:256
	s_bcnt1_i32_b64 s18, s[40:41]
	s_bcnt1_i32_b64 s19, s[42:43]
	s_waitcnt lgkmcnt(0)
	v_cmp_eq_u32_e32 vcc, 0, v3
	s_nop 1
	v_and_b32_e32 v5, vcc_lo, v0
	v_and_b32_e32 v4, vcc_hi, v1
	v_bcnt_u32_b32 v5, v5, 0
	v_bcnt_u32_b32 v4, v4, v5
	v_add_u32_e32 v4, s2, v4
	v_cndmask_b32_e32 v4, 0, v4, vcc
	s_bcnt1_i32_b64 s22, vcc
	v_cmp_eq_u32_e32 vcc, 1, v3
	s_add_i32 s2, s2, s22
	s_bcnt1_i32_b64 s22, vcc
	v_and_b32_e32 v6, vcc_lo, v0
	v_and_b32_e32 v5, vcc_hi, v1
	v_bcnt_u32_b32 v6, v6, 0
	v_bcnt_u32_b32 v5, v5, v6
	v_add_u32_e32 v5, s3, v5
	v_cndmask_b32_e32 v4, v4, v5, vcc
	v_cmp_eq_u32_e32 vcc, 2, v3
	s_add_i32 s3, s3, s22
	s_bcnt1_i32_b64 s22, vcc
	v_and_b32_e32 v6, vcc_lo, v0
	v_and_b32_e32 v5, vcc_hi, v1
	v_bcnt_u32_b32 v6, v6, 0
	v_bcnt_u32_b32 v5, v5, v6
	v_add_u32_e32 v5, s6, v5
	v_cndmask_b32_e32 v4, v4, v5, vcc
	v_cmp_eq_u32_e32 vcc, 3, v3
	s_add_i32 s22, s6, s22
	s_bcnt1_i32_b64 s6, vcc
	v_and_b32_e32 v6, vcc_lo, v0
	v_and_b32_e32 v5, vcc_hi, v1
	v_bcnt_u32_b32 v6, v6, 0
	v_bcnt_u32_b32 v5, v5, v6
	v_add_u32_e32 v5, s7, v5
	v_cndmask_b32_e32 v4, v4, v5, vcc
	v_cmp_eq_u32_e32 vcc, 4, v3
	s_add_i32 s23, s7, s6
	s_bcnt1_i32_b64 s6, vcc
	v_and_b32_e32 v6, vcc_lo, v0
	v_and_b32_e32 v5, vcc_hi, v1
	v_bcnt_u32_b32 v6, v6, 0
	v_bcnt_u32_b32 v5, v5, v6
	v_add_u32_e32 v5, s10, v5
	v_cndmask_b32_e32 v4, v4, v5, vcc
	v_cmp_eq_u32_e32 vcc, 5, v3
	s_add_i32 s31, s10, s6
	s_bcnt1_i32_b64 s6, vcc
	v_and_b32_e32 v6, vcc_lo, v0
	v_and_b32_e32 v5, vcc_hi, v1
	v_bcnt_u32_b32 v6, v6, 0
	v_bcnt_u32_b32 v5, v5, v6
	v_add_u32_e32 v5, s11, v5
	v_cndmask_b32_e32 v4, v4, v5, vcc
	v_cmp_eq_u32_e32 vcc, 6, v3
	v_cmp_eq_u32_e64 s[38:39], 7, v3
	s_add_i32 s33, s11, s6
	v_and_b32_e32 v6, vcc_lo, v0
	v_and_b32_e32 v5, vcc_hi, v1
	v_bcnt_u32_b32 v6, v6, 0
	v_bcnt_u32_b32 v5, v5, v6
	v_add_u32_e32 v5, s18, v5
	v_cndmask_b32_e32 v4, v4, v5, vcc
	v_and_b32_e32 v5, s38, v0
	v_and_b32_e32 v3, s39, v1
	v_bcnt_u32_b32 v5, v5, 0
	v_bcnt_u32_b32 v3, v3, v5
	v_add_u32_e32 v3, s19, v3
	v_cndmask_b32_e64 v3, v4, v3, s[38:39]
	ds_write_b32 v2, v3 offset:1280
	ds_read_b32 v3, v2 offset:512
	s_bcnt1_i32_b64 s6, vcc
	s_add_i32 s40, s18, s6
	s_bcnt1_i32_b64 s6, s[38:39]
	s_add_i32 s41, s19, s6
	s_waitcnt lgkmcnt(0)
	v_cmp_eq_u32_e32 vcc, 0, v3
	s_bcnt1_i32_b64 s6, vcc
	s_add_i32 s6, s2, s6
	v_and_b32_e32 v5, vcc_lo, v0
	v_and_b32_e32 v4, vcc_hi, v1
	v_bcnt_u32_b32 v5, v5, 0
	v_bcnt_u32_b32 v4, v4, v5
	v_add_u32_e32 v4, s2, v4
	v_cndmask_b32_e32 v4, 0, v4, vcc
	v_cmp_eq_u32_e32 vcc, 1, v3
	s_bcnt1_i32_b64 s2, vcc
	s_add_i32 s7, s3, s2
	v_and_b32_e32 v6, vcc_lo, v0
	v_and_b32_e32 v5, vcc_hi, v1
	v_bcnt_u32_b32 v6, v6, 0
	v_bcnt_u32_b32 v5, v5, v6
	v_add_u32_e32 v5, s3, v5
	v_cndmask_b32_e32 v4, v4, v5, vcc
	v_cmp_eq_u32_e32 vcc, 2, v3
	s_bcnt1_i32_b64 s2, vcc
	s_add_i32 s10, s22, s2
	v_and_b32_e32 v6, vcc_lo, v0
	v_and_b32_e32 v5, vcc_hi, v1
	v_bcnt_u32_b32 v6, v6, 0
	v_bcnt_u32_b32 v5, v5, v6
	v_add_u32_e32 v5, s22, v5
	v_cndmask_b32_e32 v4, v4, v5, vcc
	v_cmp_eq_u32_e32 vcc, 3, v3
	s_bcnt1_i32_b64 s2, vcc
	s_add_i32 s11, s23, s2
	v_and_b32_e32 v6, vcc_lo, v0
	v_and_b32_e32 v5, vcc_hi, v1
	v_bcnt_u32_b32 v6, v6, 0
	v_bcnt_u32_b32 v5, v5, v6
	v_add_u32_e32 v5, s23, v5
	v_cndmask_b32_e32 v4, v4, v5, vcc
	v_cmp_eq_u32_e32 vcc, 4, v3
	s_bcnt1_i32_b64 s2, vcc
	s_add_i32 s18, s31, s2
	v_and_b32_e32 v6, vcc_lo, v0
	v_and_b32_e32 v5, vcc_hi, v1
	v_bcnt_u32_b32 v6, v6, 0
	v_bcnt_u32_b32 v5, v5, v6
	v_add_u32_e32 v5, s31, v5
	v_cndmask_b32_e32 v4, v4, v5, vcc
	v_cmp_eq_u32_e32 vcc, 5, v3
	s_bcnt1_i32_b64 s2, vcc
	v_cmp_eq_u32_e64 s[38:39], 7, v3
	v_and_b32_e32 v6, vcc_lo, v0
	v_and_b32_e32 v5, vcc_hi, v1
	v_bcnt_u32_b32 v6, v6, 0
	v_bcnt_u32_b32 v5, v5, v6
	v_add_u32_e32 v5, s33, v5
	v_cndmask_b32_e32 v4, v4, v5, vcc
	v_cmp_eq_u32_e32 vcc, 6, v3
	v_and_b32_e32 v3, s39, v1
	s_add_i32 s19, s33, s2
	v_and_b32_e32 v6, vcc_lo, v0
	v_and_b32_e32 v5, vcc_hi, v1
	v_bcnt_u32_b32 v6, v6, 0
	v_bcnt_u32_b32 v5, v5, v6
	v_add_u32_e32 v5, s40, v5
	v_cndmask_b32_e32 v4, v4, v5, vcc
	v_and_b32_e32 v5, s38, v0
	v_bcnt_u32_b32 v5, v5, 0
	v_bcnt_u32_b32 v3, v3, v5
	v_add_u32_e32 v3, s41, v3
	v_cndmask_b32_e64 v3, v4, v3, s[38:39]
	ds_write_b32 v2, v3 offset:1536
	ds_read_b32 v3, v2 offset:768
	s_bcnt1_i32_b64 s2, vcc
	s_add_i32 s22, s40, s2
	s_bcnt1_i32_b64 s2, s[38:39]
	s_add_i32 s23, s41, s2
	s_waitcnt lgkmcnt(0)
	v_cmp_eq_u32_e32 vcc, 0, v3
	v_cmp_eq_u32_e64 s[38:39], 1, v3
	v_cmp_eq_u32_e64 s[40:41], 2, v3
	v_and_b32_e32 v5, vcc_lo, v0
	v_and_b32_e32 v4, vcc_hi, v1
	v_bcnt_u32_b32 v5, v5, 0
	v_and_b32_e32 v6, s38, v0
	v_bcnt_u32_b32 v4, v4, v5
	v_and_b32_e32 v5, s39, v1
	v_bcnt_u32_b32 v6, v6, 0
	v_add_u32_e32 v4, s6, v4
	v_bcnt_u32_b32 v5, v5, v6
	v_cndmask_b32_e32 v4, 0, v4, vcc
	v_add_u32_e32 v5, s7, v5
	v_and_b32_e32 v6, s40, v0
	v_cndmask_b32_e64 v4, v4, v5, s[38:39]
	v_and_b32_e32 v5, s41, v1
	v_bcnt_u32_b32 v6, v6, 0
	v_bcnt_u32_b32 v5, v5, v6
	v_cmp_eq_u32_e64 s[42:43], 3, v3
	v_add_u32_e32 v5, s10, v5
	v_cndmask_b32_e64 v4, v4, v5, s[40:41]
	v_and_b32_e32 v6, s42, v0
	v_and_b32_e32 v5, s43, v1
	v_bcnt_u32_b32 v6, v6, 0
	v_bcnt_u32_b32 v5, v5, v6
	v_cmp_eq_u32_e64 s[44:45], 4, v3
	v_add_u32_e32 v5, s11, v5
	v_cndmask_b32_e64 v4, v4, v5, s[42:43]
	v_and_b32_e32 v6, s44, v0
	v_and_b32_e32 v5, s45, v1
	v_bcnt_u32_b32 v6, v6, 0
	v_bcnt_u32_b32 v5, v5, v6
	v_cmp_eq_u32_e64 s[46:47], 5, v3
	v_add_u32_e32 v5, s18, v5
	v_cndmask_b32_e64 v4, v4, v5, s[44:45]
	v_and_b32_e32 v6, s46, v0
	v_and_b32_e32 v5, s47, v1
	v_bcnt_u32_b32 v6, v6, 0
	v_bcnt_u32_b32 v5, v5, v6
	v_cmp_eq_u32_e64 s[48:49], 6, v3
	v_add_u32_e32 v5, s19, v5
	v_cmp_eq_u32_e64 s[50:51], 7, v3
	v_and_b32_e32 v6, s48, v0
	v_cndmask_b32_e64 v4, v4, v5, s[46:47]
	v_and_b32_e32 v5, s49, v1
	v_bcnt_u32_b32 v6, v6, 0
	v_and_b32_e32 v0, s50, v0
	v_bcnt_u32_b32 v5, v5, v6
	v_and_b32_e32 v1, s51, v1
	v_bcnt_u32_b32 v0, v0, 0
	v_add_u32_e32 v5, s22, v5
	v_bcnt_u32_b32 v0, v1, v0
	v_cndmask_b32_e64 v4, v4, v5, s[48:49]
	v_add_u32_e32 v0, s23, v0
	v_cndmask_b32_e64 v0, v4, v0, s[50:51]
	ds_write_b32 v2, v0 offset:1792
	s_and_saveexec_b64 s[2:3], s[54:55]
	s_cbranch_execz .LBB0_1398
	s_bcnt1_i32_b64 s31, s[50:51]
	s_add_i32 s23, s23, s31
	s_bcnt1_i32_b64 s31, s[48:49]
	s_add_i32 s22, s22, s31
	s_bcnt1_i32_b64 s31, s[46:47]
	s_add_i32 s19, s19, s31
	s_bcnt1_i32_b64 s31, s[44:45]
	s_add_i32 s18, s18, s31
	s_bcnt1_i32_b64 s31, s[42:43]
	s_add_i32 s11, s11, s31
	s_bcnt1_i32_b64 s31, s[40:41]
	s_add_i32 s10, s10, s31
	s_bcnt1_i32_b64 s31, s[38:39]
	s_add_i32 s7, s7, s31
	s_bcnt1_i32_b64 s31, vcc
	s_add_i32 s6, s6, s31
	v_mov_b32_e32 v0, s6
	v_cndmask_b32_e64 v0, 0, v0, s[36:37]
	v_mov_b32_e32 v1, s7
	v_cmp_eq_u32_e32 vcc, 1, v144
	v_readlane_b32 s6, v252, 7
	s_nop 0
	v_cndmask_b32_e32 v0, v0, v1, vcc
	v_mov_b32_e32 v1, s10
	v_cmp_eq_u32_e32 vcc, 2, v144
	s_nop 1
	v_cndmask_b32_e32 v0, v0, v1, vcc
	v_mov_b32_e32 v1, s11
	v_cmp_eq_u32_e32 vcc, 3, v144
	s_nop 1
	v_cndmask_b32_e32 v0, v0, v1, vcc
	v_mov_b32_e32 v1, s18
	v_cmp_eq_u32_e32 vcc, 4, v144
	s_nop 1
	v_cndmask_b32_e32 v0, v0, v1, vcc
	v_mov_b32_e32 v1, s19
	v_cmp_eq_u32_e32 vcc, 5, v144
	s_nop 1
	v_cndmask_b32_e32 v0, v0, v1, vcc
	v_mov_b32_e32 v1, s22
	v_cmp_eq_u32_e32 vcc, 6, v144
	s_nop 1
	v_cndmask_b32_e32 v0, v0, v1, vcc
	v_mov_b32_e32 v1, s23
	v_cmp_eq_u32_e32 vcc, 7, v144
	s_nop 1
	v_cndmask_b32_e32 v2, v0, v1, vcc
	v_add_u32_e32 v0, s6, v144
	v_ashrrev_i32_e32 v1, 31, v0
	v_lshl_add_u64 v[0:1], v[0:1], 2, s[34:35]
	v_add_co_u32_e32 v0, vcc, 0x3c4000, v0
	s_nop 1
	v_addc_co_u32_e32 v1, vcc, 0, v1, vcc
	global_store_dword v[0:1], v2, off
